# adds: out-projection residual epilogue with 2-row-ahead loads and counted waits; moe loop copy also drops third-tile X loads
# speedup vs baseline: 1.0296x; 1.0097x over previous
; DI const float* resid_row(const float* H, const float* x, const float* meta, int m) {
;     if (!x) return H + (size_t)m * D;
;     const int b = m / L, t = m - b * L; return (t < NMETA) ? meta + (size_t)t * D : x + ((size_t)b * SEQ + (t - NMETA)) * D;
; }
;     DI void operator()(const f32x4 (&acc)[2][2][4][2], const Unit& u, int wr, int wc, int fr, int fq) const {
;         const int row0 = u.pm * BM + wr * 64 + fr, col0 = u.pn * BM + wc * 32 + 4 * fq;
; #pragma unroll
;         for (int ai = 0; ai < 2; ++ai)
; #pragma unroll
;             for (int m = 0; m < 4; ++m) { const int row = row0 + ai * HALF + m * 16; float* rowp = H + (size_t)row * D + col0; const float* srcp = resid_row(H, x, meta, row) + col0; f32x4 rs[2][2];
; #pragma unroll
;                 for (int bj = 0; bj < 2; ++bj)
; #pragma unroll
;                     for (int n = 0; n < 2; ++n) rs[bj][n] = *(const f32x4*)(srcp + bj * HALF + n * 16);
; #pragma unroll
;                 for (int bj = 0; bj < 2; ++bj)
; #pragma unroll
;                     for (int n = 0; n < 2; ++n) *(f32x4*)(rowp + bj * HALF + n * 16) = rs[bj][n] + acc[ai][bj][m][n]; }
;     }
.LBB0_1518:
	v_lshl_add_u32 v153, s44, 8, v149
	v_lshl_or_b32 v155, s69, 8, v151
	v_lshlrev_b32_e32 v155, 2, v155
	v_mov_b32_e32 v143, 0
	v_mov_b32_e32 v142, v155
	v_lshl_add_u64 v[144:145], s[8:9], 0, v[142:143]
	s_andn2_b64 vcc, exec, s[30:31]
	s_cbranch_vccnz .Lepires_l1
	v_lshl_add_u64 v[192:193], s[26:27], 0, v[142:143]
	v_lshl_add_u64 v[194:195], s[4:5], 0, v[142:143]
	s_mov_b32 s54, 0xfe03f81
	s_movk_i32 s55, 0xf7f0
	v_add_u32_e32 v154, 0, v153
	v_mul_hi_i32 v197, v154, s54
	v_lshrrev_b32_e32 v198, 31, v197
	v_ashrrev_i32_e32 v197, 7, v197
	v_add_u32_e32 v197, v197, v198
	v_mad_i32_i24 v198, v197, s55, v154
	v_cmp_lt_i32_e32 vcc, 15, v198
	v_lshlrev_b32_e32 v216, 13, v198
	v_add_u32_e32 v199, -16, v198
	v_lshlrev_b32_e32 v199, 13, v199
	v_lshl_add_u32 v199, v197, 24, v199
	v_cndmask_b32_e32 v142, v216, v199, vcc
	v_cndmask_b32_e32 v234, v194, v192, vcc
	v_cndmask_b32_e32 v235, v195, v193, vcc
	v_lshl_add_u64 v[172:173], v[234:235], 0, v[142:143]
	v_add_u32_e32 v154, 16, v153
	v_mul_hi_i32 v197, v154, s54
	v_lshrrev_b32_e32 v198, 31, v197
	v_ashrrev_i32_e32 v197, 7, v197
	v_add_u32_e32 v197, v197, v198
	v_mad_i32_i24 v198, v197, s55, v154
	v_cmp_lt_i32_e32 vcc, 15, v198
	v_lshlrev_b32_e32 v216, 13, v198
	v_add_u32_e32 v199, -16, v198
	v_lshlrev_b32_e32 v199, 13, v199
	v_lshl_add_u32 v199, v197, 24, v199
	v_cndmask_b32_e32 v142, v216, v199, vcc
	v_cndmask_b32_e32 v234, v194, v192, vcc
	v_cndmask_b32_e32 v235, v195, v193, vcc
	v_lshl_add_u64 v[174:175], v[234:235], 0, v[142:143]
	v_add_u32_e32 v154, 32, v153
	v_mul_hi_i32 v197, v154, s54
	v_lshrrev_b32_e32 v198, 31, v197
	v_ashrrev_i32_e32 v197, 7, v197
	v_add_u32_e32 v197, v197, v198
	v_mad_i32_i24 v198, v197, s55, v154
	v_cmp_lt_i32_e32 vcc, 15, v198
	v_lshlrev_b32_e32 v216, 13, v198
	v_add_u32_e32 v199, -16, v198
	v_lshlrev_b32_e32 v199, 13, v199
	v_lshl_add_u32 v199, v197, 24, v199
	v_cndmask_b32_e32 v142, v216, v199, vcc
	v_cndmask_b32_e32 v234, v194, v192, vcc
	v_cndmask_b32_e32 v235, v195, v193, vcc
	v_lshl_add_u64 v[176:177], v[234:235], 0, v[142:143]
	v_add_u32_e32 v154, 48, v153
	v_mul_hi_i32 v197, v154, s54
	v_lshrrev_b32_e32 v198, 31, v197
	v_ashrrev_i32_e32 v197, 7, v197
	v_add_u32_e32 v197, v197, v198
	v_mad_i32_i24 v198, v197, s55, v154
	v_cmp_lt_i32_e32 vcc, 15, v198
	v_lshlrev_b32_e32 v216, 13, v198
	v_add_u32_e32 v199, -16, v198
	v_lshlrev_b32_e32 v199, 13, v199
	v_lshl_add_u32 v199, v197, 24, v199
	v_cndmask_b32_e32 v142, v216, v199, vcc
	v_cndmask_b32_e32 v234, v194, v192, vcc
	v_cndmask_b32_e32 v235, v195, v193, vcc
	v_lshl_add_u64 v[178:179], v[234:235], 0, v[142:143]
	v_add_u32_e32 v154, 128, v153
	v_mul_hi_i32 v197, v154, s54
	v_lshrrev_b32_e32 v198, 31, v197
	v_ashrrev_i32_e32 v197, 7, v197
	v_add_u32_e32 v197, v197, v198
	v_mad_i32_i24 v198, v197, s55, v154
	v_cmp_lt_i32_e32 vcc, 15, v198
	v_lshlrev_b32_e32 v216, 13, v198
	v_add_u32_e32 v199, -16, v198
	v_lshlrev_b32_e32 v199, 13, v199
	v_lshl_add_u32 v199, v197, 24, v199
	v_cndmask_b32_e32 v142, v216, v199, vcc
	v_cndmask_b32_e32 v234, v194, v192, vcc
	v_cndmask_b32_e32 v235, v195, v193, vcc
	v_lshl_add_u64 v[180:181], v[234:235], 0, v[142:143]
	v_add_u32_e32 v154, 144, v153
	v_mul_hi_i32 v197, v154, s54
	v_lshrrev_b32_e32 v198, 31, v197
	v_ashrrev_i32_e32 v197, 7, v197
	v_add_u32_e32 v197, v197, v198
	v_mad_i32_i24 v198, v197, s55, v154
	v_cmp_lt_i32_e32 vcc, 15, v198
	v_lshlrev_b32_e32 v216, 13, v198
	v_add_u32_e32 v199, -16, v198
	v_lshlrev_b32_e32 v199, 13, v199
	v_lshl_add_u32 v199, v197, 24, v199
	v_cndmask_b32_e32 v142, v216, v199, vcc
	v_cndmask_b32_e32 v234, v194, v192, vcc
	v_cndmask_b32_e32 v235, v195, v193, vcc
	v_lshl_add_u64 v[182:183], v[234:235], 0, v[142:143]
	v_add_u32_e32 v154, 160, v153
	v_mul_hi_i32 v197, v154, s54
	v_lshrrev_b32_e32 v198, 31, v197
	v_ashrrev_i32_e32 v197, 7, v197
	v_add_u32_e32 v197, v197, v198
	v_mad_i32_i24 v198, v197, s55, v154
	v_cmp_lt_i32_e32 vcc, 15, v198
	v_lshlrev_b32_e32 v216, 13, v198
	v_add_u32_e32 v199, -16, v198
	v_lshlrev_b32_e32 v199, 13, v199
	v_lshl_add_u32 v199, v197, 24, v199
	v_cndmask_b32_e32 v142, v216, v199, vcc
	v_cndmask_b32_e32 v234, v194, v192, vcc
	v_cndmask_b32_e32 v235, v195, v193, vcc
	v_lshl_add_u64 v[184:185], v[234:235], 0, v[142:143]
	v_add_u32_e32 v154, 176, v153
	v_mul_hi_i32 v197, v154, s54
	v_lshrrev_b32_e32 v198, 31, v197
	v_ashrrev_i32_e32 v197, 7, v197
	v_add_u32_e32 v197, v197, v198
	v_mad_i32_i24 v198, v197, s55, v154
	v_cmp_lt_i32_e32 vcc, 15, v198
	v_lshlrev_b32_e32 v216, 13, v198
	v_add_u32_e32 v199, -16, v198
	v_lshlrev_b32_e32 v199, 13, v199
	v_lshl_add_u32 v199, v197, 24, v199
	v_cndmask_b32_e32 v142, v216, v199, vcc
	v_cndmask_b32_e32 v234, v194, v192, vcc
	v_cndmask_b32_e32 v235, v195, v193, vcc
	v_lshl_add_u64 v[186:187], v[234:235], 0, v[142:143]
	s_branch .Lepires_go
.Lepires_l1:
	v_add_u32_e32 v154, 0, v153
	v_lshlrev_b32_e32 v142, 13, v154
	v_lshl_add_u64 v[172:173], v[144:145], 0, v[142:143]
	v_add_u32_e32 v154, 16, v153
	v_lshlrev_b32_e32 v142, 13, v154
	v_lshl_add_u64 v[174:175], v[144:145], 0, v[142:143]
	v_add_u32_e32 v154, 32, v153
	v_lshlrev_b32_e32 v142, 13, v154
	v_lshl_add_u64 v[176:177], v[144:145], 0, v[142:143]
	v_add_u32_e32 v154, 48, v153
	v_lshlrev_b32_e32 v142, 13, v154
	v_lshl_add_u64 v[178:179], v[144:145], 0, v[142:143]
	v_add_u32_e32 v154, 128, v153
	v_lshlrev_b32_e32 v142, 13, v154
	v_lshl_add_u64 v[180:181], v[144:145], 0, v[142:143]
	v_add_u32_e32 v154, 144, v153
	v_lshlrev_b32_e32 v142, 13, v154
	v_lshl_add_u64 v[182:183], v[144:145], 0, v[142:143]
	v_add_u32_e32 v154, 160, v153
	v_lshlrev_b32_e32 v142, 13, v154
	v_lshl_add_u64 v[184:185], v[144:145], 0, v[142:143]
	v_add_u32_e32 v154, 176, v153
	v_lshlrev_b32_e32 v142, 13, v154
	v_lshl_add_u64 v[186:187], v[144:145], 0, v[142:143]
;     DI void operator()(const f32x4 (&acc)[2][2][4][2], const Unit& u, int wr, int wc, int fr, int fq) const {
;         const int row0 = u.pm * BM + wr * 64 + fr, col0 = u.pn * BM + wc * 32 + 4 * fq;
; #pragma unroll
;         for (int ai = 0; ai < 2; ++ai)
; #pragma unroll
;             for (int m = 0; m < 4; ++m) { const int row = row0 + ai * HALF + m * 16; float* rowp = H + (size_t)row * D + col0; const float* srcp = resid_row(H, x, meta, row) + col0; f32x4 rs[2][2];
; #pragma unroll
;                 for (int bj = 0; bj < 2; ++bj)
; #pragma unroll
;                     for (int n = 0; n < 2; ++n) rs[bj][n] = *(const f32x4*)(srcp + bj * HALF + n * 16);
; #pragma unroll
;                 for (int bj = 0; bj < 2; ++bj)
; #pragma unroll
;                     for (int n = 0; n < 2; ++n) *(f32x4*)(rowp + bj * HALF + n * 16) = rs[bj][n] + acc[ai][bj][m][n]; }
;     }
.Lepires_go:
	global_load_dwordx4 v[200:203], v[172:173], off
	global_load_dwordx4 v[204:207], v[172:173], off offset:64
	global_load_dwordx4 v[208:211], v[172:173], off offset:512
	global_load_dwordx4 v[212:215], v[172:173], off offset:576
	global_load_dwordx4 v[236:239], v[174:175], off
	global_load_dwordx4 v[240:243], v[174:175], off offset:64
	global_load_dwordx4 v[244:247], v[174:175], off offset:512
	global_load_dwordx4 v[248:251], v[174:175], off offset:576
	global_load_dwordx4 v[156:159], v[176:177], off
	global_load_dwordx4 v[160:163], v[176:177], off offset:64
	global_load_dwordx4 v[164:167], v[176:177], off offset:512
	global_load_dwordx4 v[188:191], v[176:177], off offset:576
	v_add_u32_e32 v154, 0, v153
	v_lshlrev_b32_e32 v142, 13, v154
	v_lshl_add_u64 v[146:147], v[144:145], 0, v[142:143]
	s_waitcnt vmcnt(11)
	v_pk_add_f32 v[128:129], v[128:129], v[200:201]
	v_pk_add_f32 v[130:131], v[130:131], v[202:203]
	s_waitcnt vmcnt(10)
	v_pk_add_f32 v[124:125], v[124:125], v[204:205]
	v_pk_add_f32 v[126:127], v[126:127], v[206:207]
	s_waitcnt vmcnt(9)
	v_pk_add_f32 v[120:121], v[120:121], v[208:209]
	v_pk_add_f32 v[122:123], v[122:123], v[210:211]
	s_waitcnt vmcnt(8)
	v_pk_add_f32 v[116:117], v[116:117], v[212:213]
	v_pk_add_f32 v[118:119], v[118:119], v[214:215]
	global_store_dwordx4 v[146:147], v[128:131], off
	global_store_dwordx4 v[146:147], v[124:127], off offset:64
	global_store_dwordx4 v[146:147], v[120:123], off offset:512
	global_store_dwordx4 v[146:147], v[116:119], off offset:576
	global_load_dwordx4 v[200:203], v[178:179], off
	global_load_dwordx4 v[204:207], v[178:179], off offset:64
	global_load_dwordx4 v[208:211], v[178:179], off offset:512
	global_load_dwordx4 v[212:215], v[178:179], off offset:576
	v_add_u32_e32 v154, 16, v153
	v_lshlrev_b32_e32 v142, 13, v154
	v_lshl_add_u64 v[146:147], v[144:145], 0, v[142:143]
	s_waitcnt vmcnt(15)
	v_pk_add_f32 v[112:113], v[112:113], v[236:237]
	v_pk_add_f32 v[114:115], v[114:115], v[238:239]
	s_waitcnt vmcnt(14)
	v_pk_add_f32 v[108:109], v[108:109], v[240:241]
	v_pk_add_f32 v[110:111], v[110:111], v[242:243]
	s_waitcnt vmcnt(13)
	v_pk_add_f32 v[104:105], v[104:105], v[244:245]
	v_pk_add_f32 v[106:107], v[106:107], v[246:247]
	s_waitcnt vmcnt(12)
	v_pk_add_f32 v[100:101], v[100:101], v[248:249]
	v_pk_add_f32 v[102:103], v[102:103], v[250:251]
	global_store_dwordx4 v[146:147], v[112:115], off
	global_store_dwordx4 v[146:147], v[108:111], off offset:64
	global_store_dwordx4 v[146:147], v[104:107], off offset:512
	global_store_dwordx4 v[146:147], v[100:103], off offset:576
	global_load_dwordx4 v[236:239], v[180:181], off
	global_load_dwordx4 v[240:243], v[180:181], off offset:64
	global_load_dwordx4 v[244:247], v[180:181], off offset:512
	global_load_dwordx4 v[248:251], v[180:181], off offset:576
	v_add_u32_e32 v154, 32, v153
	v_lshlrev_b32_e32 v142, 13, v154
	v_lshl_add_u64 v[146:147], v[144:145], 0, v[142:143]
	s_waitcnt vmcnt(19)
	v_pk_add_f32 v[96:97], v[96:97], v[156:157]
	v_pk_add_f32 v[98:99], v[98:99], v[158:159]
	s_waitcnt vmcnt(18)
	v_pk_add_f32 v[92:93], v[92:93], v[160:161]
	v_pk_add_f32 v[94:95], v[94:95], v[162:163]
	s_waitcnt vmcnt(17)
	v_pk_add_f32 v[86:87], v[86:87], v[164:165]
	v_pk_add_f32 v[88:89], v[88:89], v[166:167]
	s_waitcnt vmcnt(16)
	v_pk_add_f32 v[82:83], v[82:83], v[188:189]
	v_pk_add_f32 v[84:85], v[84:85], v[190:191]
	global_store_dwordx4 v[146:147], v[96:99], off
	global_store_dwordx4 v[146:147], v[92:95], off offset:64
	global_store_dwordx4 v[146:147], v[86:89], off offset:512
	global_store_dwordx4 v[146:147], v[82:85], off offset:576
	global_load_dwordx4 v[156:159], v[182:183], off
	global_load_dwordx4 v[160:163], v[182:183], off offset:64
	global_load_dwordx4 v[164:167], v[182:183], off offset:512
	global_load_dwordx4 v[188:191], v[182:183], off offset:576
	v_add_u32_e32 v154, 48, v153
	v_lshlrev_b32_e32 v142, 13, v154
	v_lshl_add_u64 v[146:147], v[144:145], 0, v[142:143]
	s_waitcnt vmcnt(19)
	v_pk_add_f32 v[78:79], v[78:79], v[200:201]
	v_pk_add_f32 v[80:81], v[80:81], v[202:203]
	s_waitcnt vmcnt(18)
	v_pk_add_f32 v[74:75], v[74:75], v[204:205]
	v_pk_add_f32 v[76:77], v[76:77], v[206:207]
	s_waitcnt vmcnt(17)
;     DI void operator()(const f32x4 (&acc)[2][2][4][2], const Unit& u, int wr, int wc, int fr, int fq) const {
;     ...
;             for (int m = 0; m < 4; ++m) { const int row = row0 + ai * HALF + m * 16; float* rowp = H + (size_t)row * D + col0; const float* srcp = resid_row(H, x, meta, row) + col0; f32x4 rs[2][2];
; #pragma unroll
;                 for (int bj = 0; bj < 2; ++bj)
; #pragma unroll
;                     for (int n = 0; n < 2; ++n) rs[bj][n] = *(const f32x4*)(srcp + bj * HALF + n * 16);
; #pragma unroll
;                 for (int bj = 0; bj < 2; ++bj)
; #pragma unroll
;                     for (int n = 0; n < 2; ++n) *(f32x4*)(rowp + bj * HALF + n * 16) = rs[bj][n] + acc[ai][bj][m][n]; }
	v_pk_add_f32 v[70:71], v[70:71], v[208:209]
	v_pk_add_f32 v[72:73], v[72:73], v[210:211]
	s_waitcnt vmcnt(16)
	v_pk_add_f32 v[66:67], v[66:67], v[212:213]
	v_pk_add_f32 v[68:69], v[68:69], v[214:215]
	global_store_dwordx4 v[146:147], v[78:81], off
	global_store_dwordx4 v[146:147], v[74:77], off offset:64
	global_store_dwordx4 v[146:147], v[70:73], off offset:512
	global_store_dwordx4 v[146:147], v[66:69], off offset:576
	global_load_dwordx4 v[200:203], v[184:185], off
	global_load_dwordx4 v[204:207], v[184:185], off offset:64
	global_load_dwordx4 v[208:211], v[184:185], off offset:512
	global_load_dwordx4 v[212:215], v[184:185], off offset:576
	v_add_u32_e32 v154, 128, v153
	v_lshlrev_b32_e32 v142, 13, v154
	v_lshl_add_u64 v[146:147], v[144:145], 0, v[142:143]
	s_waitcnt vmcnt(19)
	v_pk_add_f32 v[62:63], v[62:63], v[236:237]
	v_pk_add_f32 v[64:65], v[64:65], v[238:239]
	s_waitcnt vmcnt(18)
	v_pk_add_f32 v[58:59], v[58:59], v[240:241]
	v_pk_add_f32 v[60:61], v[60:61], v[242:243]
	s_waitcnt vmcnt(17)
	v_pk_add_f32 v[54:55], v[54:55], v[244:245]
	v_pk_add_f32 v[56:57], v[56:57], v[246:247]
	s_waitcnt vmcnt(16)
	v_pk_add_f32 v[50:51], v[50:51], v[248:249]
	v_pk_add_f32 v[52:53], v[52:53], v[250:251]
	global_store_dwordx4 v[146:147], v[62:65], off
	global_store_dwordx4 v[146:147], v[58:61], off offset:64
	global_store_dwordx4 v[146:147], v[54:57], off offset:512
	global_store_dwordx4 v[146:147], v[50:53], off offset:576
	global_load_dwordx4 v[236:239], v[186:187], off
	global_load_dwordx4 v[240:243], v[186:187], off offset:64
	global_load_dwordx4 v[244:247], v[186:187], off offset:512
	global_load_dwordx4 v[248:251], v[186:187], off offset:576
	v_add_u32_e32 v154, 144, v153
	v_lshlrev_b32_e32 v142, 13, v154
	v_lshl_add_u64 v[146:147], v[144:145], 0, v[142:143]
	s_waitcnt vmcnt(19)
	v_pk_add_f32 v[46:47], v[46:47], v[156:157]
	v_pk_add_f32 v[48:49], v[48:49], v[158:159]
	s_waitcnt vmcnt(18)
	v_pk_add_f32 v[42:43], v[42:43], v[160:161]
	v_pk_add_f32 v[44:45], v[44:45], v[162:163]
	s_waitcnt vmcnt(17)
	v_pk_add_f32 v[38:39], v[38:39], v[164:165]
	v_pk_add_f32 v[40:41], v[40:41], v[166:167]
	s_waitcnt vmcnt(16)
	v_pk_add_f32 v[34:35], v[34:35], v[188:189]
	v_pk_add_f32 v[36:37], v[36:37], v[190:191]
	global_store_dwordx4 v[146:147], v[46:49], off
	global_store_dwordx4 v[146:147], v[42:45], off offset:64
	global_store_dwordx4 v[146:147], v[38:41], off offset:512
	global_store_dwordx4 v[146:147], v[34:37], off offset:576
	v_add_u32_e32 v154, 160, v153
	v_lshlrev_b32_e32 v142, 13, v154
	v_lshl_add_u64 v[146:147], v[144:145], 0, v[142:143]
	s_waitcnt vmcnt(15)
	v_pk_add_f32 v[30:31], v[30:31], v[200:201]
	v_pk_add_f32 v[32:33], v[32:33], v[202:203]
	s_waitcnt vmcnt(14)
	v_pk_add_f32 v[26:27], v[26:27], v[204:205]
	v_pk_add_f32 v[28:29], v[28:29], v[206:207]
	s_waitcnt vmcnt(13)
	v_pk_add_f32 v[22:23], v[22:23], v[208:209]
	v_pk_add_f32 v[24:25], v[24:25], v[210:211]
	s_waitcnt vmcnt(12)
	v_pk_add_f32 v[18:19], v[18:19], v[212:213]
	v_pk_add_f32 v[20:21], v[20:21], v[214:215]
	global_store_dwordx4 v[146:147], v[30:33], off
	global_store_dwordx4 v[146:147], v[26:29], off offset:64
	global_store_dwordx4 v[146:147], v[22:25], off offset:512
	global_store_dwordx4 v[146:147], v[18:21], off offset:576
	v_add_u32_e32 v154, 176, v153
	v_lshlrev_b32_e32 v142, 13, v154
	v_lshl_add_u64 v[146:147], v[144:145], 0, v[142:143]
	s_waitcnt vmcnt(11)
	v_pk_add_f32 v[14:15], v[14:15], v[236:237]
	v_pk_add_f32 v[16:17], v[16:17], v[238:239]
	s_waitcnt vmcnt(10)
	v_pk_add_f32 v[10:11], v[10:11], v[240:241]
	v_pk_add_f32 v[12:13], v[12:13], v[242:243]
	s_waitcnt vmcnt(9)
	v_pk_add_f32 v[6:7], v[6:7], v[244:245]
	v_pk_add_f32 v[8:9], v[8:9], v[246:247]
	s_waitcnt vmcnt(8)
	v_pk_add_f32 v[2:3], v[2:3], v[248:249]
	v_pk_add_f32 v[4:5], v[4:5], v[250:251]
	s_andn2_b64 vcc, exec, s[42:43]
	s_mov_b64 s[2:3], -1
	global_store_dwordx4 v[146:147], v[14:17], off
	global_store_dwordx4 v[146:147], v[10:13], off offset:64
	global_store_dwordx4 v[146:147], v[6:9], off offset:512
	global_store_dwordx4 v[146:147], v[2:5], off offset:576
	s_cbranch_vccnz .LBB0_1507
	s_andn2_b64 vcc, exec, s[12:13]
	s_cbranch_vccnz .LBB0_1506
	s_barrier
	s_branch .LBB0_1506

; #define LAS __attribute__((address_space(3)))
; #define MS_WLOAD(set, t) do { _Pragma("unroll") for (int r_ = 0; r_ < 4; ++r_) wr[set][r_] = __builtin_bit_cast(f32x4, __builtin_amdgcn_raw_buffer_load_b128(wrs, (int)wvo + r_ * LDW * 4, MS_CL(t) * (64 * LDW * 4), 0)); } while (0)
; #define MS_WCOMMIT(set, bufi) do { LAS unsigned char* wb_ = lds + (bufi) * MS_TILE; _Pragma("unroll") for (int i_ = 0; i_ < 4; ++i_) { \
;             u32x2 p_; p_.x = pk2(wr[set][0][i_], wr[set][1][i_]); p_.y = pk2(wr[set][2][i_], wr[set][3][i_]); \
;             *(LAS u32x2*)(wb_ + ((i_ < 2) ? lw0 : lw1) + i_ * 128) = p_; } } while (0)
; #define MS_XSLOAD(t) do { _Pragma("unroll") for (int i_ = 0; i_ < 6; ++i_) xs[i_] = __builtin_bit_cast(bf16x8, __builtin_amdgcn_raw_buffer_load_b128(xrs, (int)xso[i_], MS_CL(t) * 128, 0)); } while (0)
; #define MS_XSWRITE(bufi) do { _Pragma("unroll") for (int i_ = 0; i_ < 6; ++i_) *(LAS bf16x8*)(xw + (bufi) * MS_XBUF + i_ * 1024 + ((i_ & 1) ? (xwo ^ 64) : xwo)) = xs[i_]; } while (0)
; #define MS_STEP(I, J, t) do { MS_WCOMMIT(J, J); MS_WLOAD(J, (t) + 3); MS_COMPUTE(I); MS_XSWRITE(J); MS_XSLOAD((t) + 2); __syncthreads(); } while (0)
;     ...
;             const LAS unsigned char* xr1 = lds + MS_XOFF + wave * MS_XWAVE + tk * 128 + (((4 + q) ^ rd_g) << 4);
;             __syncthreads();
;             MS_XSLOAD(0); MS_WLOAD(0, 0); MS_WLOAD(1, 1);
;             MS_WCOMMIT(0, 0); MS_WLOAD(0, 2);
;             MS_XSWRITE(0); MS_XSLOAD(1);
;             __syncthreads();
; #pragma unroll 1
;             for (int t = 0; t < NT; t += 2) { MS_STEP(0, 1, t); MS_STEP(1, 0, t + 1); }
.Lmoe_k_b:
	s_add_i32 s0, s0, 2
	s_min_u32 s1, s0, 28
	s_lshl_b32 s12, s1, 17
	s_add_i32 s12, s12, 0x60000
	s_waitcnt vmcnt(12)
	v_cvt_pk_bf16_f32 v164, v74, v78
	s_waitcnt vmcnt(10)
	v_cvt_pk_bf16_f32 v165, v82, v86
	v_cvt_pk_bf16_f32 v166, v75, v79
	v_cvt_pk_bf16_f32 v167, v83, v87
	v_cvt_pk_bf16_f32 v190, v76, v80
	v_cvt_pk_bf16_f32 v191, v84, v88
	v_cvt_pk_bf16_f32 v192, v77, v81
	v_cvt_pk_bf16_f32 v193, v85, v89
	buffer_load_dwordx4 v[74:77], v160, s[8:11], s12 offen
	buffer_load_dwordx4 v[78:81], v90, s[8:11], s12 offen
	buffer_load_dwordx4 v[82:85], v178, s[8:11], s12 offen
	buffer_load_dwordx4 v[86:89], v179, s[8:11], s12 offen
	v_add_u32_e32 v194, 0x4000, v188
	v_add_u32_e32 v195, 0x4000, v180
	v_add_u32_e32 v214, v173, v174
	ds_write2_b64 v194, v[164:165], v[166:167] offset1:16
	ds_write2_b64 v195, v[190:191], v[192:193] offset0:32 offset1:48
	v_add_u32_e32 v215, v176, v174
	ds_read_b128 v[164:167], v214 offset:32768
	ds_read_b128 v[190:193], v214 offset:34816
	ds_read_b128 v[198:201], v215
	ds_read_b128 v[202:205], v215 offset:2048
	ds_read_b128 v[206:209], v215 offset:4096
	ds_read_b128 v[210:213], v215 offset:6144
	s_waitcnt lgkmcnt(3)
	v_mfma_f32_16x16x32_bf16 v[152:155], v[198:201], v[164:167], v[152:155]
	v_mfma_f32_16x16x32_bf16 v[62:65], v[198:201], v[190:193], v[62:65]
	s_waitcnt lgkmcnt(2)
	v_mfma_f32_16x16x32_bf16 v[120:123], v[202:205], v[164:167], v[120:123]
	v_mfma_f32_16x16x32_bf16 v[54:57], v[202:205], v[190:193], v[54:57]
	s_waitcnt lgkmcnt(1)
	v_mfma_f32_16x16x32_bf16 v[112:115], v[206:209], v[164:167], v[112:115]
	v_mfma_f32_16x16x32_bf16 v[46:49], v[206:209], v[190:193], v[46:49]
	s_waitcnt lgkmcnt(0)
	v_mfma_f32_16x16x32_bf16 v[70:73], v[210:213], v[164:167], v[70:73]
	v_mfma_f32_16x16x32_bf16 v[38:41], v[210:213], v[190:193], v[38:41]
	ds_read_b128 v[198:201], v215 offset:8192
	ds_read_b128 v[202:205], v215 offset:10240
	ds_read_b128 v[206:209], v215 offset:12288
	ds_read_b128 v[210:213], v215 offset:14336
	s_waitcnt lgkmcnt(3)
	v_mfma_f32_16x16x32_bf16 v[148:151], v[198:201], v[164:167], v[148:151]
	v_mfma_f32_16x16x32_bf16 v[58:61], v[198:201], v[190:193], v[58:61]
	s_waitcnt lgkmcnt(2)
	v_mfma_f32_16x16x32_bf16 v[116:119], v[202:205], v[164:167], v[116:119]
	v_mfma_f32_16x16x32_bf16 v[50:53], v[202:205], v[190:193], v[50:53]
	s_waitcnt lgkmcnt(1)
	v_mfma_f32_16x16x32_bf16 v[92:95], v[206:209], v[164:167], v[92:95]
	v_mfma_f32_16x16x32_bf16 v[42:45], v[206:209], v[190:193], v[42:45]
	s_waitcnt lgkmcnt(0)
	v_mfma_f32_16x16x32_bf16 v[66:69], v[210:213], v[164:167], v[66:69]
	v_mfma_f32_16x16x32_bf16 v[34:37], v[210:213], v[190:193], v[34:37]
	v_add_u32_e32 v216, v173, v175
	ds_read_b128 v[164:167], v216 offset:32768
	ds_read_b128 v[190:193], v216 offset:34816
	v_add_u32_e32 v217, v176, v175
	ds_read_b128 v[198:201], v217
	ds_read_b128 v[202:205], v217 offset:2048
	ds_read_b128 v[206:209], v217 offset:4096
	ds_read_b128 v[210:213], v217 offset:6144
	s_waitcnt lgkmcnt(3)
	v_mfma_f32_16x16x32_bf16 v[152:155], v[198:201], v[164:167], v[152:155]
	v_mfma_f32_16x16x32_bf16 v[62:65], v[198:201], v[190:193], v[62:65]
	s_waitcnt lgkmcnt(2)
	v_mfma_f32_16x16x32_bf16 v[120:123], v[202:205], v[164:167], v[120:123]
	v_mfma_f32_16x16x32_bf16 v[54:57], v[202:205], v[190:193], v[54:57]
	s_waitcnt lgkmcnt(1)
	v_mfma_f32_16x16x32_bf16 v[112:115], v[206:209], v[164:167], v[112:115]
	v_mfma_f32_16x16x32_bf16 v[46:49], v[206:209], v[190:193], v[46:49]
	s_waitcnt lgkmcnt(0)
	v_mfma_f32_16x16x32_bf16 v[70:73], v[210:213], v[164:167], v[70:73]
	v_mfma_f32_16x16x32_bf16 v[38:41], v[210:213], v[190:193], v[38:41]
	ds_read_b128 v[198:201], v217 offset:8192
	ds_read_b128 v[202:205], v217 offset:10240
	ds_read_b128 v[206:209], v217 offset:12288
	ds_read_b128 v[210:213], v217 offset:14336
	s_min_u32 s12, s0, 29
	s_lshl_b32 s12, s12, 7
	s_waitcnt vmcnt(7)
	ds_write_b128 v189, v[132:135] offset:38912
	s_waitcnt vmcnt(6)
	ds_write_b128 v181, v[124:127] offset:39936
	s_waitcnt vmcnt(5)
	ds_write_b128 v189, v[140:143] offset:40960
	s_waitcnt vmcnt(4)
	ds_write_b128 v181, v[144:147] offset:41984
	s_addk_i32 s12, 0x100
	s_waitcnt lgkmcnt(7)
	v_mfma_f32_16x16x32_bf16 v[148:151], v[198:201], v[164:167], v[148:151]
	buffer_load_dwordx4 v[124:127], v182, s[4:7], s12 offen
	buffer_load_dwordx4 v[128:131], v183, s[4:7], s12 offen
	buffer_load_dwordx4 v[132:135], v184, s[4:7], s12 offen
	buffer_load_dwordx4 v[136:139], v185, s[4:7], s12 offen
	s_min_u32 s12, s0, 27
	s_waitcnt lgkmcnt(0)
	v_mfma_f32_16x16x32_bf16 v[116:119], v[202:205], v[164:167], v[116:119]
	s_barrier
; #define LAS __attribute__((address_space(3)))
; #define MS_WLOAD(set, t) do { _Pragma("unroll") for (int r_ = 0; r_ < 4; ++r_) wr[set][r_] = __builtin_bit_cast(f32x4, __builtin_amdgcn_raw_buffer_load_b128(wrs, (int)wvo + r_ * LDW * 4, MS_CL(t) * (64 * LDW * 4), 0)); } while (0)
; #define MS_WCOMMIT(set, bufi) do { LAS unsigned char* wb_ = lds + (bufi) * MS_TILE; _Pragma("unroll") for (int i_ = 0; i_ < 4; ++i_) { \
;             u32x2 p_; p_.x = pk2(wr[set][0][i_], wr[set][1][i_]); p_.y = pk2(wr[set][2][i_], wr[set][3][i_]); \
;             *(LAS u32x2*)(wb_ + ((i_ < 2) ? lw0 : lw1) + i_ * 128) = p_; } } while (0)
; #define MS_XSLOAD(t) do { _Pragma("unroll") for (int i_ = 0; i_ < 6; ++i_) xs[i_] = __builtin_bit_cast(bf16x8, __builtin_amdgcn_raw_buffer_load_b128(xrs, (int)xso[i_], MS_CL(t) * 128, 0)); } while (0)
; #define MS_XSWRITE(bufi) do { _Pragma("unroll") for (int i_ = 0; i_ < 6; ++i_) *(LAS bf16x8*)(xw + (bufi) * MS_XBUF + i_ * 1024 + ((i_ & 1) ? (xwo ^ 64) : xwo)) = xs[i_]; } while (0)
; #define MS_STEP(I, J, t) do { MS_WCOMMIT(J, J); MS_WLOAD(J, (t) + 3); MS_COMPUTE(I); MS_XSWRITE(J); MS_XSLOAD((t) + 2); __syncthreads(); } while (0)
;     ...
;             const LAS unsigned char* xr1 = lds + MS_XOFF + wave * MS_XWAVE + tk * 128 + (((4 + q) ^ rd_g) << 4);
;             __syncthreads();
;             MS_XSLOAD(0); MS_WLOAD(0, 0); MS_WLOAD(1, 1);
;             MS_WCOMMIT(0, 0); MS_WLOAD(0, 2);
;             MS_XSWRITE(0); MS_XSLOAD(1);
;             __syncthreads();
; #pragma unroll 1
;             for (int t = 0; t < NT; t += 2) { MS_STEP(0, 1, t); MS_STEP(1, 0, t + 1); }
	s_lshl_b32 s12, s12, 17
	v_mfma_f32_16x16x32_bf16 v[92:95], v[206:209], v[164:167], v[92:95]
	s_add_i32 s12, s12, 0x80000
	v_mfma_f32_16x16x32_bf16 v[66:69], v[210:213], v[164:167], v[66:69]
	v_cvt_pk_bf16_f32 v164, v96, v100
	v_cvt_pk_bf16_f32 v165, v104, v108
	v_cvt_pk_bf16_f32 v96, v97, v101
	v_cvt_pk_bf16_f32 v97, v105, v109
	ds_write2_b64 v188, v[164:165], v[96:97] offset1:16
	v_cvt_pk_bf16_f32 v96, v98, v102
	v_cvt_pk_bf16_f32 v97, v106, v110
	v_cvt_pk_bf16_f32 v98, v99, v103
	v_cvt_pk_bf16_f32 v99, v107, v111
	ds_write2_b64 v180, v[96:97], v[98:99] offset0:32 offset1:48
	buffer_load_dwordx4 v[96:99], v160, s[8:11], s12 offen
	buffer_load_dwordx4 v[100:103], v90, s[8:11], s12 offen
	buffer_load_dwordx4 v[104:107], v178, s[8:11], s12 offen
	buffer_load_dwordx4 v[108:111], v179, s[8:11], s12 offen
	v_mfma_f32_16x16x32_bf16 v[58:61], v[198:201], v[190:193], v[58:61]
	v_mfma_f32_16x16x32_bf16 v[50:53], v[202:205], v[190:193], v[50:53]
	v_mfma_f32_16x16x32_bf16 v[42:45], v[206:209], v[190:193], v[42:45]
	v_mfma_f32_16x16x32_bf16 v[34:37], v[210:213], v[190:193], v[34:37]
	ds_read_b128 v[164:167], v214 offset:38912
	ds_read_b128 v[190:193], v214 offset:40960
	ds_read_b128 v[198:201], v215 offset:16384
	ds_read_b128 v[202:205], v215 offset:18432
	ds_read_b128 v[206:209], v215 offset:20480
	ds_read_b128 v[210:213], v215 offset:22528
	s_waitcnt lgkmcnt(3)
	v_mfma_f32_16x16x32_bf16 v[152:155], v[198:201], v[164:167], v[152:155]
	v_mfma_f32_16x16x32_bf16 v[62:65], v[198:201], v[190:193], v[62:65]
	s_waitcnt lgkmcnt(2)
	v_mfma_f32_16x16x32_bf16 v[120:123], v[202:205], v[164:167], v[120:123]
	v_mfma_f32_16x16x32_bf16 v[54:57], v[202:205], v[190:193], v[54:57]
	s_waitcnt lgkmcnt(1)
	v_mfma_f32_16x16x32_bf16 v[112:115], v[206:209], v[164:167], v[112:115]
	v_mfma_f32_16x16x32_bf16 v[46:49], v[206:209], v[190:193], v[46:49]
	s_waitcnt lgkmcnt(0)
	v_mfma_f32_16x16x32_bf16 v[70:73], v[210:213], v[164:167], v[70:73]
	v_mfma_f32_16x16x32_bf16 v[38:41], v[210:213], v[190:193], v[38:41]
	ds_read_b128 v[198:201], v215 offset:24576
	ds_read_b128 v[202:205], v215 offset:26624
	ds_read_b128 v[206:209], v215 offset:28672
	ds_read_b128 v[210:213], v215 offset:30720
	s_waitcnt lgkmcnt(3)
	v_mfma_f32_16x16x32_bf16 v[148:151], v[198:201], v[164:167], v[148:151]
	v_mfma_f32_16x16x32_bf16 v[58:61], v[198:201], v[190:193], v[58:61]
	s_waitcnt lgkmcnt(2)
	v_mfma_f32_16x16x32_bf16 v[116:119], v[202:205], v[164:167], v[116:119]
	v_mfma_f32_16x16x32_bf16 v[50:53], v[202:205], v[190:193], v[50:53]
	s_waitcnt lgkmcnt(1)
	v_mfma_f32_16x16x32_bf16 v[92:95], v[206:209], v[164:167], v[92:95]
	v_mfma_f32_16x16x32_bf16 v[42:45], v[206:209], v[190:193], v[42:45]
	s_waitcnt lgkmcnt(0)
	v_mfma_f32_16x16x32_bf16 v[66:69], v[210:213], v[164:167], v[66:69]
	v_mfma_f32_16x16x32_bf16 v[34:37], v[210:213], v[190:193], v[34:37]
	ds_read_b128 v[164:167], v216 offset:38912
	ds_read_b128 v[190:193], v216 offset:40960
	ds_read_b128 v[198:201], v217 offset:16384
	ds_read_b128 v[202:205], v217 offset:18432
	ds_read_b128 v[206:209], v217 offset:20480
	ds_read_b128 v[210:213], v217 offset:22528
	s_waitcnt lgkmcnt(3)
	v_mfma_f32_16x16x32_bf16 v[152:155], v[198:201], v[164:167], v[152:155]
	v_mfma_f32_16x16x32_bf16 v[62:65], v[198:201], v[190:193], v[62:65]
	s_waitcnt lgkmcnt(2)
	v_mfma_f32_16x16x32_bf16 v[120:123], v[202:205], v[164:167], v[120:123]
	v_mfma_f32_16x16x32_bf16 v[54:57], v[202:205], v[190:193], v[54:57]
	s_waitcnt lgkmcnt(1)
	v_mfma_f32_16x16x32_bf16 v[112:115], v[206:209], v[164:167], v[112:115]
	v_mfma_f32_16x16x32_bf16 v[46:49], v[206:209], v[190:193], v[46:49]
	s_waitcnt lgkmcnt(0)
	v_mfma_f32_16x16x32_bf16 v[70:73], v[210:213], v[164:167], v[70:73]
	v_mfma_f32_16x16x32_bf16 v[38:41], v[210:213], v[190:193], v[38:41]
	ds_read_b128 v[198:201], v217 offset:24576
	ds_read_b128 v[202:205], v217 offset:26624
	ds_read_b128 v[206:209], v217 offset:28672
	ds_read_b128 v[210:213], v217 offset:30720
	s_lshl_b32 s1, s1, 7
	s_waitcnt vmcnt(7)
	ds_write_b128 v189, v[124:127] offset:32768
	s_waitcnt vmcnt(6)
	ds_write_b128 v181, v[128:131] offset:33792
	s_waitcnt vmcnt(5)
	ds_write_b128 v189, v[132:135] offset:34816
	s_waitcnt vmcnt(4)
	ds_write_b128 v181, v[136:139] offset:35840
	s_addk_i32 s1, 0x180
	buffer_load_dwordx4 v[132:135], v182, s[4:7], s1 offen
	buffer_load_dwordx4 v[124:127], v183, s[4:7], s1 offen
	buffer_load_dwordx4 v[140:143], v184, s[4:7], s1 offen
	buffer_load_dwordx4 v[144:147], v185, s[4:7], s1 offen
	s_waitcnt lgkmcnt(7)
	v_mfma_f32_16x16x32_bf16 v[148:151], v[198:201], v[164:167], v[148:151]
	s_cmp_gt_u32 s0, 29
	s_waitcnt lgkmcnt(0)
	s_barrier
	v_mfma_f32_16x16x32_bf16 v[58:61], v[198:201], v[190:193], v[58:61]
	v_mfma_f32_16x16x32_bf16 v[116:119], v[202:205], v[164:167], v[116:119]
	v_mfma_f32_16x16x32_bf16 v[50:53], v[202:205], v[190:193], v[50:53]
	v_mfma_f32_16x16x32_bf16 v[92:95], v[206:209], v[164:167], v[92:95]
	v_mfma_f32_16x16x32_bf16 v[42:45], v[206:209], v[190:193], v[42:45]
	v_mfma_f32_16x16x32_bf16 v[66:69], v[210:213], v[164:167], v[66:69]
	v_mfma_f32_16x16x32_bf16 v[34:37], v[210:213], v[190:193], v[34:37]
	s_cbranch_scc0 .Lmoe_k_b

; #define LAS __attribute__((address_space(3)))
; #define MS_WLOAD(set, t) do { _Pragma("unroll") for (int r_ = 0; r_ < 4; ++r_) wr[set][r_] = __builtin_bit_cast(f32x4, __builtin_amdgcn_raw_buffer_load_b128(wrs, (int)wvo + r_ * LDW * 4, MS_CL(t) * (64 * LDW * 4), 0)); } while (0)
; #define MS_WCOMMIT(set, bufi) do { LAS unsigned char* wb_ = lds + (bufi) * MS_TILE; _Pragma("unroll") for (int i_ = 0; i_ < 4; ++i_) { \
;             u32x2 p_; p_.x = pk2(wr[set][0][i_], wr[set][1][i_]); p_.y = pk2(wr[set][2][i_], wr[set][3][i_]); \
;             *(LAS u32x2*)(wb_ + ((i_ < 2) ? lw0 : lw1) + i_ * 128) = p_; } } while (0)
; #define MS_XSLOAD(t) do { _Pragma("unroll") for (int i_ = 0; i_ < 6; ++i_) xs[i_] = __builtin_bit_cast(bf16x8, __builtin_amdgcn_raw_buffer_load_b128(xrs, (int)xso[i_], MS_CL(t) * 128, 0)); } while (0)
; #define MS_XSWRITE(bufi) do { _Pragma("unroll") for (int i_ = 0; i_ < 6; ++i_) *(LAS bf16x8*)(xw + (bufi) * MS_XBUF + i_ * 1024 + ((i_ & 1) ? (xwo ^ 64) : xwo)) = xs[i_]; } while (0)
; #define MS_STEP(I, J, t) do { MS_WCOMMIT(J, J); MS_WLOAD(J, (t) + 3); MS_COMPUTE(I); MS_XSWRITE(J); MS_XSLOAD((t) + 2); __syncthreads(); } while (0)
;     ...
;             const LAS unsigned char* xr1 = lds + MS_XOFF + wave * MS_XWAVE + tk * 128 + (((4 + q) ^ rd_g) << 4);
;             __syncthreads();
;             MS_XSLOAD(0); MS_WLOAD(0, 0); MS_WLOAD(1, 1);
;             MS_WCOMMIT(0, 0); MS_WLOAD(0, 2);
;             MS_XSWRITE(0); MS_XSLOAD(1);
;             __syncthreads();
; #pragma unroll 1
;             for (int t = 0; t < NT; t += 2) { MS_STEP(0, 1, t); MS_STEP(1, 0, t + 1); }
.Lmoe_l_b:
	s_add_i32 s2, s2, 2
	s_min_u32 s3, s2, 4
	s_lshl_b32 s33, s3, 19
	s_add_i32 s33, s33, 0x180000
	s_waitcnt vmcnt(10)
	v_cvt_pk_bf16_f32 v164, v2, v10
	s_waitcnt vmcnt(7)
	v_cvt_pk_bf16_f32 v165, v6, v14
	v_cvt_pk_bf16_f32 v166, v3, v11
	v_cvt_pk_bf16_f32 v167, v7, v15
	v_cvt_pk_bf16_f32 v190, v4, v12
	v_cvt_pk_bf16_f32 v191, v8, v16
	v_cvt_pk_bf16_f32 v192, v5, v13
	v_cvt_pk_bf16_f32 v193, v9, v17
	buffer_load_dwordx4 v[2:5], v160, s[8:11], s33 offen
	buffer_load_dwordx4 v[10:13], v90, s[8:11], s33 offen
	buffer_load_dwordx4 v[6:9], v178, s[8:11], s33 offen
	buffer_load_dwordx4 v[14:17], v179, s[8:11], s33 offen
	v_add_u32_e32 v194, 0x4000, v188
	v_add_u32_e32 v195, 0x4000, v180
	v_add_u32_e32 v214, v173, v174
	ds_write2_b64 v194, v[164:165], v[166:167] offset1:16
	ds_write2_b64 v195, v[190:191], v[192:193] offset0:32 offset1:48
	v_add_u32_e32 v215, v176, v174
	ds_read_b128 v[164:167], v214 offset:32768
	ds_read_b128 v[190:193], v214 offset:34816
	ds_read_b128 v[198:201], v215
	ds_read_b128 v[202:205], v215 offset:2048
	ds_read_b128 v[206:209], v215 offset:4096
	ds_read_b128 v[210:213], v215 offset:6144
	s_waitcnt lgkmcnt(3)
	v_mfma_f32_16x16x32_bf16 v[152:155], v[198:201], v[164:167], v[152:155]
	v_mfma_f32_16x16x32_bf16 v[120:123], v[198:201], v[190:193], v[120:123]
	s_waitcnt lgkmcnt(2)
	v_mfma_f32_16x16x32_bf16 v[148:151], v[202:205], v[164:167], v[148:151]
	v_mfma_f32_16x16x32_bf16 v[96:99], v[202:205], v[190:193], v[96:99]
	s_waitcnt lgkmcnt(1)
	v_mfma_f32_16x16x32_bf16 v[144:147], v[206:209], v[164:167], v[144:147]
	v_mfma_f32_16x16x32_bf16 v[86:89], v[206:209], v[190:193], v[86:89]
	s_waitcnt lgkmcnt(0)
	v_mfma_f32_16x16x32_bf16 v[140:143], v[210:213], v[164:167], v[140:143]
	v_mfma_f32_16x16x32_bf16 v[82:85], v[210:213], v[190:193], v[82:85]
	ds_read_b128 v[198:201], v215 offset:8192
	ds_read_b128 v[202:205], v215 offset:10240
	ds_read_b128 v[206:209], v215 offset:12288
	ds_read_b128 v[210:213], v215 offset:14336
	s_waitcnt lgkmcnt(3)
	v_mfma_f32_16x16x32_bf16 v[136:139], v[198:201], v[164:167], v[136:139]
	v_mfma_f32_16x16x32_bf16 v[78:81], v[198:201], v[190:193], v[78:81]
	s_waitcnt lgkmcnt(2)
	v_mfma_f32_16x16x32_bf16 v[132:135], v[202:205], v[164:167], v[132:135]
	v_mfma_f32_16x16x32_bf16 v[74:77], v[202:205], v[190:193], v[74:77]
	s_waitcnt lgkmcnt(1)
	v_mfma_f32_16x16x32_bf16 v[128:131], v[206:209], v[164:167], v[128:131]
	v_mfma_f32_16x16x32_bf16 v[70:73], v[206:209], v[190:193], v[70:73]
	s_waitcnt lgkmcnt(0)
	v_mfma_f32_16x16x32_bf16 v[124:127], v[210:213], v[164:167], v[124:127]
	v_mfma_f32_16x16x32_bf16 v[66:69], v[210:213], v[190:193], v[66:69]
	v_add_u32_e32 v216, v173, v175
	ds_read_b128 v[164:167], v216 offset:32768
	ds_read_b128 v[190:193], v216 offset:34816
	v_add_u32_e32 v217, v176, v175
	ds_read_b128 v[198:201], v217
	ds_read_b128 v[202:205], v217 offset:2048
	ds_read_b128 v[206:209], v217 offset:4096
	ds_read_b128 v[210:213], v217 offset:6144
	s_waitcnt lgkmcnt(3)
	v_mfma_f32_16x16x32_bf16 v[152:155], v[198:201], v[164:167], v[152:155]
	v_mfma_f32_16x16x32_bf16 v[120:123], v[198:201], v[190:193], v[120:123]
	s_waitcnt lgkmcnt(2)
	v_mfma_f32_16x16x32_bf16 v[148:151], v[202:205], v[164:167], v[148:151]
	v_mfma_f32_16x16x32_bf16 v[96:99], v[202:205], v[190:193], v[96:99]
	s_waitcnt lgkmcnt(1)
	v_mfma_f32_16x16x32_bf16 v[144:147], v[206:209], v[164:167], v[144:147]
	v_mfma_f32_16x16x32_bf16 v[86:89], v[206:209], v[190:193], v[86:89]
	s_waitcnt lgkmcnt(0)
	v_mfma_f32_16x16x32_bf16 v[140:143], v[210:213], v[164:167], v[140:143]
	v_mfma_f32_16x16x32_bf16 v[82:85], v[210:213], v[190:193], v[82:85]
	ds_read_b128 v[198:201], v217 offset:8192
	ds_read_b128 v[202:205], v217 offset:10240
	ds_read_b128 v[206:209], v217 offset:12288
	ds_read_b128 v[210:213], v217 offset:14336
	s_min_u32 s33, s2, 5
	s_lshl_b32 s33, s33, 7
	s_waitcnt vmcnt(7)
	ds_write_b128 v189, v[104:107] offset:38912
	s_waitcnt vmcnt(6)
	ds_write_b128 v181, v[92:95] offset:39936
	s_waitcnt vmcnt(5)
	ds_write_b128 v189, v[112:115] offset:40960
	s_waitcnt vmcnt(4)
	ds_write_b128 v181, v[116:119] offset:41984
	s_addk_i32 s33, 0x100
	s_waitcnt lgkmcnt(7)
	v_mfma_f32_16x16x32_bf16 v[136:139], v[198:201], v[164:167], v[136:139]
	buffer_load_dwordx4 v[92:95], v182, s[4:7], s33 offen
	buffer_load_dwordx4 v[100:103], v183, s[4:7], s33 offen
	buffer_load_dwordx4 v[104:107], v184, s[4:7], s33 offen
	buffer_load_dwordx4 v[108:111], v185, s[4:7], s33 offen
	s_min_u32 s33, s2, 3
	s_waitcnt lgkmcnt(0)
	v_mfma_f32_16x16x32_bf16 v[132:135], v[202:205], v[164:167], v[132:135]
	s_barrier
; #define LAS __attribute__((address_space(3)))
; #define MS_WLOAD(set, t) do { _Pragma("unroll") for (int r_ = 0; r_ < 4; ++r_) wr[set][r_] = __builtin_bit_cast(f32x4, __builtin_amdgcn_raw_buffer_load_b128(wrs, (int)wvo + r_ * LDW * 4, MS_CL(t) * (64 * LDW * 4), 0)); } while (0)
; #define MS_WCOMMIT(set, bufi) do { LAS unsigned char* wb_ = lds + (bufi) * MS_TILE; _Pragma("unroll") for (int i_ = 0; i_ < 4; ++i_) { \
;             u32x2 p_; p_.x = pk2(wr[set][0][i_], wr[set][1][i_]); p_.y = pk2(wr[set][2][i_], wr[set][3][i_]); \
;             *(LAS u32x2*)(wb_ + ((i_ < 2) ? lw0 : lw1) + i_ * 128) = p_; } } while (0)
; #define MS_XSLOAD(t) do { _Pragma("unroll") for (int i_ = 0; i_ < 6; ++i_) xs[i_] = __builtin_bit_cast(bf16x8, __builtin_amdgcn_raw_buffer_load_b128(xrs, (int)xso[i_], MS_CL(t) * 128, 0)); } while (0)
; #define MS_XSWRITE(bufi) do { _Pragma("unroll") for (int i_ = 0; i_ < 6; ++i_) *(LAS bf16x8*)(xw + (bufi) * MS_XBUF + i_ * 1024 + ((i_ & 1) ? (xwo ^ 64) : xwo)) = xs[i_]; } while (0)
; #define MS_STEP(I, J, t) do { MS_WCOMMIT(J, J); MS_WLOAD(J, (t) + 3); MS_COMPUTE(I); MS_XSWRITE(J); MS_XSLOAD((t) + 2); __syncthreads(); } while (0)
;     ...
;             const LAS unsigned char* xr1 = lds + MS_XOFF + wave * MS_XWAVE + tk * 128 + (((4 + q) ^ rd_g) << 4);
;             __syncthreads();
;             MS_XSLOAD(0); MS_WLOAD(0, 0); MS_WLOAD(1, 1);
;             MS_WCOMMIT(0, 0); MS_WLOAD(0, 2);
;             MS_XSWRITE(0); MS_XSLOAD(1);
;             __syncthreads();
; #pragma unroll 1
;             for (int t = 0; t < NT; t += 2) { MS_STEP(0, 1, t); MS_STEP(1, 0, t + 1); }
	s_lshl_b32 s33, s33, 19
	v_mfma_f32_16x16x32_bf16 v[128:131], v[206:209], v[164:167], v[128:131]
	s_bitset1_b32 s33, 21
	v_mfma_f32_16x16x32_bf16 v[124:127], v[210:213], v[164:167], v[124:127]
	v_cvt_pk_bf16_f32 v164, v18, v22
	v_cvt_pk_bf16_f32 v165, v26, v30
	v_cvt_pk_bf16_f32 v18, v19, v23
	v_cvt_pk_bf16_f32 v19, v27, v31
	ds_write2_b64 v188, v[164:165], v[18:19] offset1:16
	v_cvt_pk_bf16_f32 v18, v20, v24
	v_cvt_pk_bf16_f32 v19, v28, v32
	v_cvt_pk_bf16_f32 v20, v21, v25
	v_cvt_pk_bf16_f32 v21, v29, v33
	ds_write2_b64 v180, v[18:19], v[20:21] offset0:32 offset1:48
	buffer_load_dwordx4 v[18:21], v160, s[8:11], s33 offen
	buffer_load_dwordx4 v[22:25], v90, s[8:11], s33 offen
	buffer_load_dwordx4 v[26:29], v178, s[8:11], s33 offen
	buffer_load_dwordx4 v[30:33], v179, s[8:11], s33 offen
	v_mfma_f32_16x16x32_bf16 v[78:81], v[198:201], v[190:193], v[78:81]
	v_mfma_f32_16x16x32_bf16 v[74:77], v[202:205], v[190:193], v[74:77]
	v_mfma_f32_16x16x32_bf16 v[70:73], v[206:209], v[190:193], v[70:73]
	v_mfma_f32_16x16x32_bf16 v[66:69], v[210:213], v[190:193], v[66:69]
	ds_read_b128 v[164:167], v214 offset:38912
	ds_read_b128 v[190:193], v214 offset:40960
	ds_read_b128 v[198:201], v215 offset:16384
	ds_read_b128 v[202:205], v215 offset:18432
	ds_read_b128 v[206:209], v215 offset:20480
	ds_read_b128 v[210:213], v215 offset:22528
	s_waitcnt lgkmcnt(3)
	v_mfma_f32_16x16x32_bf16 v[152:155], v[198:201], v[164:167], v[152:155]
	v_mfma_f32_16x16x32_bf16 v[120:123], v[198:201], v[190:193], v[120:123]
	s_waitcnt lgkmcnt(2)
	v_mfma_f32_16x16x32_bf16 v[148:151], v[202:205], v[164:167], v[148:151]
	v_mfma_f32_16x16x32_bf16 v[96:99], v[202:205], v[190:193], v[96:99]
	s_waitcnt lgkmcnt(1)
	v_mfma_f32_16x16x32_bf16 v[144:147], v[206:209], v[164:167], v[144:147]
	v_mfma_f32_16x16x32_bf16 v[86:89], v[206:209], v[190:193], v[86:89]
	s_waitcnt lgkmcnt(0)
	v_mfma_f32_16x16x32_bf16 v[140:143], v[210:213], v[164:167], v[140:143]
	v_mfma_f32_16x16x32_bf16 v[82:85], v[210:213], v[190:193], v[82:85]
	ds_read_b128 v[198:201], v215 offset:24576
	ds_read_b128 v[202:205], v215 offset:26624
	ds_read_b128 v[206:209], v215 offset:28672
	ds_read_b128 v[210:213], v215 offset:30720
	s_waitcnt lgkmcnt(3)
	v_mfma_f32_16x16x32_bf16 v[136:139], v[198:201], v[164:167], v[136:139]
	v_mfma_f32_16x16x32_bf16 v[78:81], v[198:201], v[190:193], v[78:81]
	s_waitcnt lgkmcnt(2)
	v_mfma_f32_16x16x32_bf16 v[132:135], v[202:205], v[164:167], v[132:135]
	v_mfma_f32_16x16x32_bf16 v[74:77], v[202:205], v[190:193], v[74:77]
	s_waitcnt lgkmcnt(1)
	v_mfma_f32_16x16x32_bf16 v[128:131], v[206:209], v[164:167], v[128:131]
	v_mfma_f32_16x16x32_bf16 v[70:73], v[206:209], v[190:193], v[70:73]
	s_waitcnt lgkmcnt(0)
	v_mfma_f32_16x16x32_bf16 v[124:127], v[210:213], v[164:167], v[124:127]
	v_mfma_f32_16x16x32_bf16 v[66:69], v[210:213], v[190:193], v[66:69]
	ds_read_b128 v[164:167], v216 offset:38912
	ds_read_b128 v[190:193], v216 offset:40960
	ds_read_b128 v[198:201], v217 offset:16384
	ds_read_b128 v[202:205], v217 offset:18432
	ds_read_b128 v[206:209], v217 offset:20480
	ds_read_b128 v[210:213], v217 offset:22528
	s_waitcnt lgkmcnt(3)
	v_mfma_f32_16x16x32_bf16 v[152:155], v[198:201], v[164:167], v[152:155]
	v_mfma_f32_16x16x32_bf16 v[120:123], v[198:201], v[190:193], v[120:123]
	s_waitcnt lgkmcnt(2)
	v_mfma_f32_16x16x32_bf16 v[148:151], v[202:205], v[164:167], v[148:151]
	v_mfma_f32_16x16x32_bf16 v[96:99], v[202:205], v[190:193], v[96:99]
	s_waitcnt lgkmcnt(1)
	v_mfma_f32_16x16x32_bf16 v[144:147], v[206:209], v[164:167], v[144:147]
	v_mfma_f32_16x16x32_bf16 v[86:89], v[206:209], v[190:193], v[86:89]
	s_waitcnt lgkmcnt(0)
	v_mfma_f32_16x16x32_bf16 v[140:143], v[210:213], v[164:167], v[140:143]
	v_mfma_f32_16x16x32_bf16 v[82:85], v[210:213], v[190:193], v[82:85]
	ds_read_b128 v[198:201], v217 offset:24576
	ds_read_b128 v[202:205], v217 offset:26624
	ds_read_b128 v[206:209], v217 offset:28672
	ds_read_b128 v[210:213], v217 offset:30720
	s_lshl_b32 s3, s3, 7
	s_waitcnt vmcnt(7)
	ds_write_b128 v189, v[92:95] offset:32768
	s_waitcnt vmcnt(6)
	ds_write_b128 v181, v[100:103] offset:33792
	s_waitcnt vmcnt(5)
	ds_write_b128 v189, v[104:107] offset:34816
	s_waitcnt vmcnt(4)
	ds_write_b128 v181, v[108:111] offset:35840
	s_addk_i32 s3, 0x180
	buffer_load_dwordx4 v[104:107], v182, s[4:7], s3 offen
	buffer_load_dwordx4 v[92:95], v183, s[4:7], s3 offen
	buffer_load_dwordx4 v[112:115], v184, s[4:7], s3 offen
	buffer_load_dwordx4 v[116:119], v185, s[4:7], s3 offen
	s_waitcnt lgkmcnt(7)
	v_mfma_f32_16x16x32_bf16 v[136:139], v[198:201], v[164:167], v[136:139]
	s_cmp_gt_u32 s2, 5
	s_waitcnt lgkmcnt(0)
	s_barrier
	v_mfma_f32_16x16x32_bf16 v[78:81], v[198:201], v[190:193], v[78:81]
	v_mfma_f32_16x16x32_bf16 v[132:135], v[202:205], v[164:167], v[132:135]
	v_mfma_f32_16x16x32_bf16 v[74:77], v[202:205], v[190:193], v[74:77]
	v_mfma_f32_16x16x32_bf16 v[128:131], v[206:209], v[164:167], v[128:131]
	v_mfma_f32_16x16x32_bf16 v[70:73], v[206:209], v[190:193], v[70:73]
	v_mfma_f32_16x16x32_bf16 v[124:127], v[210:213], v[164:167], v[124:127]
	v_mfma_f32_16x16x32_bf16 v[66:69], v[210:213], v[190:193], v[66:69]
	s_cbranch_scc0 .Lmoe_l_b
